# balanced DMA issue + saddr-form LDS-DMA loads (no 64-bit VALU adds in the GEMM load segments)
# speedup vs baseline: 1.0102x; 1.0031x over previous
.LBB0_200:
	s_add_u32 s72, s42, 0xfff80000
	s_addc_u32 s73, s43, -1
	s_mov_b32 m0, s57
	s_nop 0
	global_load_lds_dwordx4 v160, s[72:73]
	s_mov_b32 m0, s58
	s_nop 0
	global_load_lds_dwordx4 v164, s[72:73]
	ds_read_b128 v[16:19], v186
	ds_read_b128 v[20:23], v187
	ds_read_b128 v[24:27], v188
	ds_read_b128 v[28:31], v189
	ds_read_b128 v[0:3], v190
	ds_read_b128 v[4:7], v191
	ds_read_b128 v[8:11], v192
	ds_read_b128 v[12:15], v193
	s_add_u32 s44, s42, 0xfff80080
	s_addc_u32 s45, s43, -1
	s_cmp_eq_u32 s68, 28
	s_cselect_b32 s47, s31, s45
	s_cselect_b32 s46, s35, s44
	s_cselect_b32 s45, s29, s67
	s_cselect_b32 s44, s39, s66
	s_add_i32 m0, s27, 0xc000
	ds_read_b128 v[178:181], v218
	ds_read_b128 v[182:185], v218 offset:1024
	ds_read_b128 v[222:225], v218 offset:2048
	ds_read_b128 v[226:229], v218 offset:3072
	ds_read_b128 v[230:233], v218 offset:4096
	ds_read_b128 v[234:237], v218 offset:5120
	ds_read_b128 v[238:241], v218 offset:6144
	ds_read_b128 v[242:245], v218 offset:7168
	global_load_lds_dwordx4 v172, s[42:43]
	s_add_i32 m0, s27, 0xe000
	s_nop 0
	global_load_lds_dwordx4 v174, s[42:43]
	s_waitcnt vmcnt(8)
	s_waitcnt lgkmcnt(0)
	s_barrier
	s_setprio 1
	s_waitcnt lgkmcnt(0)
	v_mfma_f32_16x16x128_f8f6f4 v[156:159], v[16:23], v[178:185], v[156:159]
	v_mfma_f32_16x16x128_f8f6f4 v[152:155], v[24:31], v[178:185], v[152:155]
	v_mfma_f32_16x16x128_f8f6f4 v[148:151], v[16:23], v[222:229], v[148:151]
	v_mfma_f32_16x16x128_f8f6f4 v[144:147], v[24:31], v[222:229], v[144:147]
	v_mfma_f32_16x16x128_f8f6f4 v[140:143], v[16:23], v[230:237], v[140:143]
	v_mfma_f32_16x16x128_f8f6f4 v[136:139], v[24:31], v[230:237], v[136:139]
	v_mfma_f32_16x16x128_f8f6f4 v[132:135], v[16:23], v[238:245], v[132:135]
	v_mfma_f32_16x16x128_f8f6f4 v[128:131], v[24:31], v[238:245], v[128:131]
	s_setprio 0
	s_setprio 1
	v_mfma_f32_16x16x128_f8f6f4 v[124:127], v[0:7], v[178:185], v[124:127]
	v_mfma_f32_16x16x128_f8f6f4 v[120:123], v[8:15], v[178:185], v[120:123]
	v_mfma_f32_16x16x128_f8f6f4 v[116:119], v[0:7], v[222:229], v[116:119]
	v_mfma_f32_16x16x128_f8f6f4 v[112:115], v[8:15], v[222:229], v[112:115]
	v_mfma_f32_16x16x128_f8f6f4 v[108:111], v[0:7], v[230:237], v[108:111]
	v_mfma_f32_16x16x128_f8f6f4 v[104:107], v[8:15], v[230:237], v[104:107]
	v_mfma_f32_16x16x128_f8f6f4 v[100:103], v[0:7], v[238:245], v[100:103]
	v_mfma_f32_16x16x128_f8f6f4 v[96:99], v[8:15], v[238:245], v[96:99]
	s_setprio 0
	s_barrier
	s_mov_b32 m0, s33
	v_lshl_add_u64 v[178:179], s[44:45], 0, v[162:163]
	s_add_u32 s70, s44, 0x80000
	ds_read_b128 v[222:225], v218 offset:16384
	ds_read_b128 v[226:229], v218 offset:17408
	ds_read_b128 v[230:233], v218 offset:18432
	ds_read_b128 v[234:237], v218 offset:19456
	ds_read_b128 v[238:241], v218 offset:20480
	ds_read_b128 v[242:245], v218 offset:21504
	ds_read_b128 v[246:249], v218 offset:22528
	ds_read_b128 v[250:253], v218 offset:23552
	global_load_lds_dwordx4 v[178:179], off
	v_lshl_add_u64 v[180:181], s[44:45], 0, v[166:167]
	s_mov_b32 m0, s48
	s_addc_u32 s71, s45, 0
	global_load_lds_dwordx4 v[180:181], off
	s_mov_b32 m0, s49
	s_nop 0
	global_load_lds_dwordx4 v162, s[70:71]
	s_mov_b32 m0, s50
	s_nop 0
	global_load_lds_dwordx4 v166, s[70:71]
	s_waitcnt vmcnt(6)
	s_waitcnt lgkmcnt(0)
	s_barrier
	s_setprio 1
	s_waitcnt lgkmcnt(0)
	v_mfma_f32_16x16x128_f8f6f4 v[92:95], v[16:23], v[222:229], v[92:95]
	v_mfma_f32_16x16x128_f8f6f4 v[88:91], v[24:31], v[222:229], v[88:91]
	v_mfma_f32_16x16x128_f8f6f4 v[84:87], v[16:23], v[230:237], v[84:87]
	v_mfma_f32_16x16x128_f8f6f4 v[80:83], v[24:31], v[230:237], v[80:83]
	v_mfma_f32_16x16x128_f8f6f4 v[76:79], v[16:23], v[238:245], v[76:79]
	v_mfma_f32_16x16x128_f8f6f4 v[72:75], v[24:31], v[238:245], v[72:75]
	v_mfma_f32_16x16x128_f8f6f4 v[68:71], v[16:23], v[246:253], v[68:71]
	v_mfma_f32_16x16x128_f8f6f4 v[64:67], v[24:31], v[246:253], v[64:67]
	s_setprio 0
	s_setprio 1
	v_mfma_f32_16x16x128_f8f6f4 v[60:63], v[0:7], v[222:229], v[60:63]
	v_mfma_f32_16x16x128_f8f6f4 v[56:59], v[8:15], v[222:229], v[56:59]
	v_mfma_f32_16x16x128_f8f6f4 v[52:55], v[0:7], v[230:237], v[52:55]
	v_mfma_f32_16x16x128_f8f6f4 v[48:51], v[8:15], v[230:237], v[48:51]
	v_mfma_f32_16x16x128_f8f6f4 v[44:47], v[0:7], v[238:245], v[44:47]
	v_mfma_f32_16x16x128_f8f6f4 v[40:43], v[8:15], v[238:245], v[40:43]
	v_mfma_f32_16x16x128_f8f6f4 v[36:39], v[0:7], v[246:253], v[36:39]
	v_mfma_f32_16x16x128_f8f6f4 v[32:35], v[8:15], v[246:253], v[32:35]
	s_setprio 0
	s_barrier
	s_mov_b32 m0, s27
	s_nop 0
	global_load_lds_dwordx4 v160, s[46:47]
	s_mov_b32 m0, s51
	s_nop 0
	global_load_lds_dwordx4 v164, s[46:47]
	ds_read_b128 v[0:3], v194
	ds_read_b128 v[4:7], v195
	ds_read_b128 v[8:11], v196
	ds_read_b128 v[12:15], v197
	ds_read_b128 v[16:19], v198
	ds_read_b128 v[20:23], v199
	ds_read_b128 v[24:27], v200
	ds_read_b128 v[28:31], v201
	s_add_u32 s46, s46, 0x80000
	s_addc_u32 s47, s47, 0
	s_mov_b32 m0, s52
	ds_read_b128 v[222:225], v218 offset:32768
	ds_read_b128 v[226:229], v218 offset:33792
	ds_read_b128 v[230:233], v218 offset:34816
	ds_read_b128 v[234:237], v218 offset:35840
	ds_read_b128 v[238:241], v218 offset:36864
	ds_read_b128 v[242:245], v218 offset:37888
	ds_read_b128 v[246:249], v218 offset:38912
	ds_read_b128 v[250:253], v218 offset:39936
	global_load_lds_dwordx4 v160, s[46:47]
	s_mov_b32 m0, s53
	s_nop 0
	global_load_lds_dwordx4 v164, s[46:47]
	s_waitcnt vmcnt(8)
	s_waitcnt lgkmcnt(0)
	s_barrier
	s_setprio 1
	s_waitcnt lgkmcnt(0)
	v_mfma_f32_16x16x128_f8f6f4 v[156:159], v[0:7], v[222:229], v[156:159]
	v_mfma_f32_16x16x128_f8f6f4 v[152:155], v[8:15], v[222:229], v[152:155]
	v_mfma_f32_16x16x128_f8f6f4 v[148:151], v[0:7], v[230:237], v[148:151]
	v_mfma_f32_16x16x128_f8f6f4 v[144:147], v[8:15], v[230:237], v[144:147]
	v_mfma_f32_16x16x128_f8f6f4 v[140:143], v[0:7], v[238:245], v[140:143]
	v_mfma_f32_16x16x128_f8f6f4 v[136:139], v[8:15], v[238:245], v[136:139]
	v_mfma_f32_16x16x128_f8f6f4 v[132:135], v[0:7], v[246:253], v[132:135]
	v_mfma_f32_16x16x128_f8f6f4 v[128:131], v[8:15], v[246:253], v[128:131]
	s_setprio 0
	s_setprio 1
	v_mfma_f32_16x16x128_f8f6f4 v[124:127], v[16:23], v[222:229], v[124:127]
	v_mfma_f32_16x16x128_f8f6f4 v[120:123], v[24:31], v[222:229], v[120:123]
	v_mfma_f32_16x16x128_f8f6f4 v[116:119], v[16:23], v[230:237], v[116:119]
	v_mfma_f32_16x16x128_f8f6f4 v[112:115], v[24:31], v[230:237], v[112:115]
	v_mfma_f32_16x16x128_f8f6f4 v[108:111], v[16:23], v[238:245], v[108:111]
	v_mfma_f32_16x16x128_f8f6f4 v[104:107], v[24:31], v[238:245], v[104:107]
	v_mfma_f32_16x16x128_f8f6f4 v[100:103], v[16:23], v[246:253], v[100:103]
	v_mfma_f32_16x16x128_f8f6f4 v[96:99], v[24:31], v[246:253], v[96:99]
	s_setprio 0
	s_barrier
	s_mov_b32 m0, s55
	v_lshl_add_u64 v[176:177], v[178:179], 0, s[20:21]
	s_add_u32 s44, s44, 0x80080
	ds_read_b128 v[222:225], v218 offset:49152
	ds_read_b128 v[226:229], v218 offset:50176
	ds_read_b128 v[230:233], v218 offset:51200
	ds_read_b128 v[234:237], v218 offset:52224
	ds_read_b128 v[238:241], v218 offset:53248
	ds_read_b128 v[242:245], v218 offset:54272
	ds_read_b128 v[246:249], v218 offset:55296
	ds_read_b128 v[250:253], v218 offset:56320
	global_load_lds_dwordx4 v[176:177], off
	v_lshl_add_u64 v[176:177], v[180:181], 0, s[20:21]
	s_mov_b32 m0, s56
	s_addc_u32 s45, s45, 0
	global_load_lds_dwordx4 v[176:177], off
	s_mov_b32 m0, s59
	s_nop 0
	global_load_lds_dwordx4 v162, s[44:45]
	s_mov_b32 m0, s60
	s_nop 0
	global_load_lds_dwordx4 v166, s[44:45]
	s_waitcnt vmcnt(6)
	s_waitcnt lgkmcnt(0)
	s_barrier
	s_setprio 1
	s_waitcnt lgkmcnt(0)
	v_mfma_f32_16x16x128_f8f6f4 v[92:95], v[0:7], v[222:229], v[92:95]
	v_mfma_f32_16x16x128_f8f6f4 v[88:91], v[8:15], v[222:229], v[88:91]
	v_mfma_f32_16x16x128_f8f6f4 v[84:87], v[0:7], v[230:237], v[84:87]
	v_mfma_f32_16x16x128_f8f6f4 v[80:83], v[8:15], v[230:237], v[80:83]
	v_mfma_f32_16x16x128_f8f6f4 v[76:79], v[0:7], v[238:245], v[76:79]
	v_mfma_f32_16x16x128_f8f6f4 v[72:75], v[8:15], v[238:245], v[72:75]
	v_mfma_f32_16x16x128_f8f6f4 v[68:71], v[0:7], v[246:253], v[68:71]
	v_mfma_f32_16x16x128_f8f6f4 v[64:67], v[8:15], v[246:253], v[64:67]
	s_setprio 0
	s_setprio 1
	v_mfma_f32_16x16x128_f8f6f4 v[60:63], v[16:23], v[222:229], v[60:63]
	v_mfma_f32_16x16x128_f8f6f4 v[56:59], v[24:31], v[222:229], v[56:59]
	v_mfma_f32_16x16x128_f8f6f4 v[52:55], v[16:23], v[230:237], v[52:55]
	v_mfma_f32_16x16x128_f8f6f4 v[48:51], v[24:31], v[230:237], v[48:51]
	v_mfma_f32_16x16x128_f8f6f4 v[44:47], v[16:23], v[238:245], v[44:47]
	v_mfma_f32_16x16x128_f8f6f4 v[40:43], v[24:31], v[238:245], v[40:43]
	v_mfma_f32_16x16x128_f8f6f4 v[36:39], v[16:23], v[246:253], v[36:39]
	v_mfma_f32_16x16x128_f8f6f4 v[32:35], v[24:31], v[246:253], v[32:35]
	s_setprio 0
	s_barrier
	s_add_i32 s68, s68, 2
	s_add_u32 s42, s42, 0x100
	s_addc_u32 s43, s43, 0
	s_add_u32 s66, s66, 0x100
	s_addc_u32 s67, s67, 0
	s_cmp_gt_u32 s68, 29
	s_cbranch_scc0 .LBB0_200
	s_nop 15
	s_nop 15
	s_and_b64 vcc, exec, s[22:23]
	s_cbranch_vccz .LBB0_203
	s_barrier

.LBB0_562:
	s_add_u32 s72, s30, 0xfff80000
	s_addc_u32 s73, s31, -1
	s_mov_b32 m0, s49
	s_nop 0
	global_load_lds_dwordx4 v160, s[72:73]
	s_mov_b32 m0, s50
	s_nop 0
	global_load_lds_dwordx4 v162, s[72:73]
	ds_read_b128 v[16:19], v181
	ds_read_b128 v[20:23], v182
	ds_read_b128 v[24:27], v183
	ds_read_b128 v[28:31], v184
	ds_read_b128 v[0:3], v185
	ds_read_b128 v[4:7], v186
	ds_read_b128 v[8:11], v187
	ds_read_b128 v[12:15], v188
	s_add_u32 s34, s30, 0xfff80080
	s_addc_u32 s35, s31, -1
	s_cmp_eq_u32 s59, 28
	s_cselect_b32 s37, s23, s35
	s_cselect_b32 s36, s55, s34
	s_cselect_b32 s35, s21, s58
	s_cselect_b32 s34, s56, s57
	s_add_i32 m0, s29, 0xc000
	ds_read_b128 v[172:175], v198
	ds_read_b128 v[176:179], v198 offset:1024
	ds_read_b128 v[200:203], v198 offset:2048
	ds_read_b128 v[204:207], v198 offset:3072
	ds_read_b128 v[208:211], v198 offset:4096
	ds_read_b128 v[212:215], v198 offset:5120
	ds_read_b128 v[216:219], v198 offset:6144
	ds_read_b128 v[220:223], v198 offset:7168
	global_load_lds_dwordx4 v164, s[30:31]
	s_add_i32 m0, s29, 0xe000
	s_nop 0
	global_load_lds_dwordx4 v166, s[30:31]
	s_waitcnt vmcnt(8)
	s_waitcnt lgkmcnt(0)
	s_barrier
	s_setprio 1
	s_waitcnt lgkmcnt(0)
	v_mfma_f32_16x16x128_f8f6f4 v[156:159], v[16:23], v[172:179], v[156:159]
	v_mfma_f32_16x16x128_f8f6f4 v[152:155], v[24:31], v[172:179], v[152:155]
	v_mfma_f32_16x16x128_f8f6f4 v[148:151], v[16:23], v[200:207], v[148:151]
	v_mfma_f32_16x16x128_f8f6f4 v[144:147], v[24:31], v[200:207], v[144:147]
	v_mfma_f32_16x16x128_f8f6f4 v[124:127], v[16:23], v[208:215], v[124:127]
	v_mfma_f32_16x16x128_f8f6f4 v[120:123], v[24:31], v[208:215], v[120:123]
	v_mfma_f32_16x16x128_f8f6f4 v[116:119], v[16:23], v[216:223], v[116:119]
	v_mfma_f32_16x16x128_f8f6f4 v[112:115], v[24:31], v[216:223], v[112:115]
	s_setprio 0
	s_setprio 1
	v_mfma_f32_16x16x128_f8f6f4 v[140:143], v[0:7], v[172:179], v[140:143]
	v_mfma_f32_16x16x128_f8f6f4 v[136:139], v[8:15], v[172:179], v[136:139]
	v_mfma_f32_16x16x128_f8f6f4 v[132:135], v[0:7], v[200:207], v[132:135]
	v_mfma_f32_16x16x128_f8f6f4 v[128:131], v[8:15], v[200:207], v[128:131]
	v_mfma_f32_16x16x128_f8f6f4 v[108:111], v[0:7], v[208:215], v[108:111]
	v_mfma_f32_16x16x128_f8f6f4 v[104:107], v[8:15], v[208:215], v[104:107]
	v_mfma_f32_16x16x128_f8f6f4 v[100:103], v[0:7], v[216:223], v[100:103]
	v_mfma_f32_16x16x128_f8f6f4 v[96:99], v[8:15], v[216:223], v[96:99]
	s_setprio 0
	s_barrier
	s_mov_b32 m0, s33
	v_lshl_add_u64 v[172:173], s[34:35], 0, v[160:161]
	s_add_u32 s60, s34, 0x80000
	ds_read_b128 v[200:203], v198 offset:16384
	ds_read_b128 v[204:207], v198 offset:17408
	ds_read_b128 v[208:211], v198 offset:18432
	ds_read_b128 v[212:215], v198 offset:19456
	ds_read_b128 v[216:219], v198 offset:20480
	ds_read_b128 v[220:223], v198 offset:21504
	ds_read_b128 v[224:227], v198 offset:22528
	ds_read_b128 v[228:231], v198 offset:23552
	global_load_lds_dwordx4 v[172:173], off
	v_lshl_add_u64 v[174:175], s[34:35], 0, v[162:163]
	s_mov_b32 m0, s38
	s_addc_u32 s61, s35, 0
	global_load_lds_dwordx4 v[174:175], off
	s_mov_b32 m0, s39
	s_nop 0
	global_load_lds_dwordx4 v160, s[60:61]
	s_mov_b32 m0, s40
	s_nop 0
	global_load_lds_dwordx4 v162, s[60:61]
	s_waitcnt vmcnt(6)
	s_waitcnt lgkmcnt(0)
	s_barrier
	s_setprio 1
	s_waitcnt lgkmcnt(0)
	v_mfma_f32_16x16x128_f8f6f4 v[92:95], v[16:23], v[200:207], v[92:95]
	v_mfma_f32_16x16x128_f8f6f4 v[88:91], v[24:31], v[200:207], v[88:91]
	v_mfma_f32_16x16x128_f8f6f4 v[84:87], v[16:23], v[208:215], v[84:87]
	v_mfma_f32_16x16x128_f8f6f4 v[80:83], v[24:31], v[208:215], v[80:83]
	v_mfma_f32_16x16x128_f8f6f4 v[60:63], v[16:23], v[216:223], v[60:63]
	v_mfma_f32_16x16x128_f8f6f4 v[56:59], v[24:31], v[216:223], v[56:59]
	v_mfma_f32_16x16x128_f8f6f4 v[52:55], v[16:23], v[224:231], v[52:55]
	v_mfma_f32_16x16x128_f8f6f4 v[48:51], v[24:31], v[224:231], v[48:51]
	s_setprio 0
	s_setprio 1
	v_mfma_f32_16x16x128_f8f6f4 v[76:79], v[0:7], v[200:207], v[76:79]
	v_mfma_f32_16x16x128_f8f6f4 v[72:75], v[8:15], v[200:207], v[72:75]
	v_mfma_f32_16x16x128_f8f6f4 v[68:71], v[0:7], v[208:215], v[68:71]
	v_mfma_f32_16x16x128_f8f6f4 v[64:67], v[8:15], v[208:215], v[64:67]
	v_mfma_f32_16x16x128_f8f6f4 v[44:47], v[0:7], v[216:223], v[44:47]
	v_mfma_f32_16x16x128_f8f6f4 v[40:43], v[8:15], v[216:223], v[40:43]
	v_mfma_f32_16x16x128_f8f6f4 v[36:39], v[0:7], v[224:231], v[36:39]
	v_mfma_f32_16x16x128_f8f6f4 v[32:35], v[8:15], v[224:231], v[32:35]
	s_setprio 0
	s_barrier
	s_mov_b32 m0, s29
	s_nop 0
	global_load_lds_dwordx4 v160, s[36:37]
	s_mov_b32 m0, s41
	s_nop 0
	global_load_lds_dwordx4 v162, s[36:37]
	ds_read_b128 v[0:3], v189
	ds_read_b128 v[4:7], v190
	ds_read_b128 v[8:11], v191
	ds_read_b128 v[12:15], v192
	ds_read_b128 v[16:19], v193
	ds_read_b128 v[20:23], v194
	ds_read_b128 v[24:27], v195
	ds_read_b128 v[28:31], v196
	s_add_u32 s36, s36, 0x80000
	s_addc_u32 s37, s37, 0
	s_mov_b32 m0, s42
	ds_read_b128 v[200:203], v198 offset:32768
	ds_read_b128 v[204:207], v198 offset:33792
	ds_read_b128 v[208:211], v198 offset:34816
	ds_read_b128 v[212:215], v198 offset:35840
	ds_read_b128 v[216:219], v198 offset:36864
	ds_read_b128 v[220:223], v198 offset:37888
	ds_read_b128 v[224:227], v198 offset:38912
	ds_read_b128 v[228:231], v198 offset:39936
	global_load_lds_dwordx4 v160, s[36:37]
	s_mov_b32 m0, s43
	s_nop 0
	global_load_lds_dwordx4 v162, s[36:37]
	s_waitcnt vmcnt(8)
	s_waitcnt lgkmcnt(0)
	s_barrier
	s_setprio 1
	s_waitcnt lgkmcnt(0)
	v_mfma_f32_16x16x128_f8f6f4 v[156:159], v[0:7], v[200:207], v[156:159]
	v_mfma_f32_16x16x128_f8f6f4 v[152:155], v[8:15], v[200:207], v[152:155]
	v_mfma_f32_16x16x128_f8f6f4 v[148:151], v[0:7], v[208:215], v[148:151]
	v_mfma_f32_16x16x128_f8f6f4 v[144:147], v[8:15], v[208:215], v[144:147]
	v_mfma_f32_16x16x128_f8f6f4 v[124:127], v[0:7], v[216:223], v[124:127]
	v_mfma_f32_16x16x128_f8f6f4 v[120:123], v[8:15], v[216:223], v[120:123]
	v_mfma_f32_16x16x128_f8f6f4 v[116:119], v[0:7], v[224:231], v[116:119]
	v_mfma_f32_16x16x128_f8f6f4 v[112:115], v[8:15], v[224:231], v[112:115]
	s_setprio 0
	s_setprio 1
	v_mfma_f32_16x16x128_f8f6f4 v[140:143], v[16:23], v[200:207], v[140:143]
	v_mfma_f32_16x16x128_f8f6f4 v[136:139], v[24:31], v[200:207], v[136:139]
	v_mfma_f32_16x16x128_f8f6f4 v[132:135], v[16:23], v[208:215], v[132:135]
	v_mfma_f32_16x16x128_f8f6f4 v[128:131], v[24:31], v[208:215], v[128:131]
	v_mfma_f32_16x16x128_f8f6f4 v[108:111], v[16:23], v[216:223], v[108:111]
	v_mfma_f32_16x16x128_f8f6f4 v[104:107], v[24:31], v[216:223], v[104:107]
	v_mfma_f32_16x16x128_f8f6f4 v[100:103], v[16:23], v[224:231], v[100:103]
	v_mfma_f32_16x16x128_f8f6f4 v[96:99], v[24:31], v[224:231], v[96:99]
	s_setprio 0
	s_barrier
	s_mov_b32 m0, s47
	v_lshl_add_u64 v[172:173], v[172:173], 0, s[14:15]
	s_add_u32 s34, s34, 0x80080
	ds_read_b128 v[200:203], v198 offset:49152
	ds_read_b128 v[204:207], v198 offset:50176
	ds_read_b128 v[208:211], v198 offset:51200
	ds_read_b128 v[212:215], v198 offset:52224
	ds_read_b128 v[216:219], v198 offset:53248
	ds_read_b128 v[220:223], v198 offset:54272
	ds_read_b128 v[224:227], v198 offset:55296
	ds_read_b128 v[228:231], v198 offset:56320
	global_load_lds_dwordx4 v[172:173], off
	v_lshl_add_u64 v[172:173], v[174:175], 0, s[14:15]
	s_mov_b32 m0, s48
	s_addc_u32 s35, s35, 0
	global_load_lds_dwordx4 v[172:173], off
	s_mov_b32 m0, s51
	s_nop 0
	global_load_lds_dwordx4 v160, s[34:35]
	s_mov_b32 m0, s52
	s_nop 0
	global_load_lds_dwordx4 v162, s[34:35]
	s_waitcnt vmcnt(6)
	s_waitcnt lgkmcnt(0)
	s_barrier
	s_setprio 1
	s_waitcnt lgkmcnt(0)
	v_mfma_f32_16x16x128_f8f6f4 v[92:95], v[0:7], v[200:207], v[92:95]
	v_mfma_f32_16x16x128_f8f6f4 v[88:91], v[8:15], v[200:207], v[88:91]
	v_mfma_f32_16x16x128_f8f6f4 v[84:87], v[0:7], v[208:215], v[84:87]
	v_mfma_f32_16x16x128_f8f6f4 v[80:83], v[8:15], v[208:215], v[80:83]
	v_mfma_f32_16x16x128_f8f6f4 v[60:63], v[0:7], v[216:223], v[60:63]
	v_mfma_f32_16x16x128_f8f6f4 v[56:59], v[8:15], v[216:223], v[56:59]
	v_mfma_f32_16x16x128_f8f6f4 v[52:55], v[0:7], v[224:231], v[52:55]
	v_mfma_f32_16x16x128_f8f6f4 v[48:51], v[8:15], v[224:231], v[48:51]
	s_setprio 0
	s_setprio 1
	v_mfma_f32_16x16x128_f8f6f4 v[76:79], v[16:23], v[200:207], v[76:79]
	v_mfma_f32_16x16x128_f8f6f4 v[72:75], v[24:31], v[200:207], v[72:75]
	v_mfma_f32_16x16x128_f8f6f4 v[68:71], v[16:23], v[208:215], v[68:71]
	v_mfma_f32_16x16x128_f8f6f4 v[64:67], v[24:31], v[208:215], v[64:67]
	v_mfma_f32_16x16x128_f8f6f4 v[44:47], v[16:23], v[216:223], v[44:47]
	v_mfma_f32_16x16x128_f8f6f4 v[40:43], v[24:31], v[216:223], v[40:43]
	v_mfma_f32_16x16x128_f8f6f4 v[36:39], v[16:23], v[224:231], v[36:39]
	v_mfma_f32_16x16x128_f8f6f4 v[32:35], v[24:31], v[224:231], v[32:35]
	s_setprio 0
	s_barrier
	s_add_i32 s59, s59, 2
	s_add_u32 s30, s30, 0x100
	s_addc_u32 s31, s31, 0
	s_add_u32 s57, s57, 0x100
	s_addc_u32 s58, s58, 0
	s_cmp_gt_u32 s59, 29
	s_cbranch_scc0 .LBB0_562
	s_nop 15
	s_nop 15
	s_and_b64 vcc, exec, s[16:17]
	s_cbranch_vccz .LBB0_565
	s_barrier

.LBB0_940:
	s_add_u32 s72, s38, 0xfff80000
	s_addc_u32 s73, s39, -1
	s_mov_b32 m0, s53
	s_nop 0
	global_load_lds_dwordx4 v160, s[72:73]
	s_mov_b32 m0, s54
	s_nop 0
	global_load_lds_dwordx4 v164, s[72:73]
	ds_read_b128 v[16:19], v189
	ds_read_b128 v[20:23], v190
	ds_read_b128 v[24:27], v191
	ds_read_b128 v[28:31], v192
	ds_read_b128 v[0:3], v193
	ds_read_b128 v[4:7], v194
	ds_read_b128 v[8:11], v195
	ds_read_b128 v[12:15], v196
	s_add_u32 s40, s38, 0xfff80080
	s_addc_u32 s41, s39, -1
	s_cmp_eq_u32 s64, 28
	s_cselect_b32 s43, s27, s41
	s_cselect_b32 s42, s35, s40
	s_cselect_b32 s41, s25, s61
	s_cselect_b32 s40, s37, s60
	s_add_i32 m0, s33, 0xc000
	ds_read_b128 v[180:183], v205
	ds_read_b128 v[184:187], v205 offset:1024
	ds_read_b128 v[208:211], v205 offset:2048
	ds_read_b128 v[212:215], v205 offset:3072
	ds_read_b128 v[216:219], v205 offset:4096
	ds_read_b128 v[220:223], v205 offset:5120
	ds_read_b128 v[224:227], v205 offset:6144
	ds_read_b128 v[228:231], v205 offset:7168
	global_load_lds_dwordx4 v172, s[38:39]
	s_add_i32 m0, s33, 0xe000
	s_nop 0
	global_load_lds_dwordx4 v174, s[38:39]
	s_waitcnt vmcnt(8)
	s_waitcnt lgkmcnt(0)
	s_barrier
	s_setprio 1
	s_waitcnt lgkmcnt(0)
	v_mfma_f32_16x16x128_f8f6f4 v[156:159], v[16:23], v[180:187], v[156:159]
	v_mfma_f32_16x16x128_f8f6f4 v[152:155], v[24:31], v[180:187], v[152:155]
	v_mfma_f32_16x16x128_f8f6f4 v[140:143], v[16:23], v[208:215], v[140:143]
	v_mfma_f32_16x16x128_f8f6f4 v[136:139], v[24:31], v[208:215], v[136:139]
	v_mfma_f32_16x16x128_f8f6f4 v[124:127], v[16:23], v[216:223], v[124:127]
	v_mfma_f32_16x16x128_f8f6f4 v[120:123], v[24:31], v[216:223], v[120:123]
	v_mfma_f32_16x16x128_f8f6f4 v[108:111], v[16:23], v[224:231], v[108:111]
	v_mfma_f32_16x16x128_f8f6f4 v[104:107], v[24:31], v[224:231], v[104:107]
	s_setprio 0
	s_setprio 1
	v_mfma_f32_16x16x128_f8f6f4 v[148:151], v[0:7], v[180:187], v[148:151]
	v_mfma_f32_16x16x128_f8f6f4 v[144:147], v[8:15], v[180:187], v[144:147]
	v_mfma_f32_16x16x128_f8f6f4 v[132:135], v[0:7], v[208:215], v[132:135]
	v_mfma_f32_16x16x128_f8f6f4 v[128:131], v[8:15], v[208:215], v[128:131]
	v_mfma_f32_16x16x128_f8f6f4 v[116:119], v[0:7], v[216:223], v[116:119]
	v_mfma_f32_16x16x128_f8f6f4 v[112:115], v[8:15], v[216:223], v[112:115]
	v_mfma_f32_16x16x128_f8f6f4 v[100:103], v[0:7], v[224:231], v[100:103]
	v_mfma_f32_16x16x128_f8f6f4 v[96:99], v[8:15], v[224:231], v[96:99]
	s_setprio 0
	s_barrier
	s_mov_b32 m0, s44
	v_lshl_add_u64 v[180:181], s[40:41], 0, v[162:163]
	s_add_u32 s62, s40, 0x80000
	ds_read_b128 v[208:211], v205 offset:16384
	ds_read_b128 v[212:215], v205 offset:17408
	ds_read_b128 v[216:219], v205 offset:18432
	ds_read_b128 v[220:223], v205 offset:19456
	ds_read_b128 v[224:227], v205 offset:20480
	ds_read_b128 v[228:231], v205 offset:21504
	ds_read_b128 v[232:235], v205 offset:22528
	ds_read_b128 v[236:239], v205 offset:23552
	global_load_lds_dwordx4 v[180:181], off
	v_lshl_add_u64 v[182:183], s[40:41], 0, v[166:167]
	s_mov_b32 m0, s45
	s_addc_u32 s63, s41, 0
	global_load_lds_dwordx4 v[182:183], off
	s_mov_b32 m0, s46
	s_nop 0
	global_load_lds_dwordx4 v162, s[62:63]
	s_mov_b32 m0, s47
	s_nop 0
	global_load_lds_dwordx4 v166, s[62:63]
	s_waitcnt vmcnt(6)
	s_waitcnt lgkmcnt(0)
	s_barrier
	s_setprio 1
	s_waitcnt lgkmcnt(0)
	v_mfma_f32_16x16x128_f8f6f4 v[92:95], v[16:23], v[208:215], v[92:95]
	v_mfma_f32_16x16x128_f8f6f4 v[88:91], v[24:31], v[208:215], v[88:91]
	v_mfma_f32_16x16x128_f8f6f4 v[76:79], v[16:23], v[216:223], v[76:79]
	v_mfma_f32_16x16x128_f8f6f4 v[72:75], v[24:31], v[216:223], v[72:75]
	v_mfma_f32_16x16x128_f8f6f4 v[60:63], v[16:23], v[224:231], v[60:63]
	v_mfma_f32_16x16x128_f8f6f4 v[56:59], v[24:31], v[224:231], v[56:59]
	v_mfma_f32_16x16x128_f8f6f4 v[44:47], v[16:23], v[232:239], v[44:47]
	v_mfma_f32_16x16x128_f8f6f4 v[40:43], v[24:31], v[232:239], v[40:43]
	s_setprio 0
	s_setprio 1
	v_mfma_f32_16x16x128_f8f6f4 v[84:87], v[0:7], v[208:215], v[84:87]
	v_mfma_f32_16x16x128_f8f6f4 v[80:83], v[8:15], v[208:215], v[80:83]
	v_mfma_f32_16x16x128_f8f6f4 v[68:71], v[0:7], v[216:223], v[68:71]
	v_mfma_f32_16x16x128_f8f6f4 v[64:67], v[8:15], v[216:223], v[64:67]
	v_mfma_f32_16x16x128_f8f6f4 v[52:55], v[0:7], v[224:231], v[52:55]
	v_mfma_f32_16x16x128_f8f6f4 v[48:51], v[8:15], v[224:231], v[48:51]
	v_mfma_f32_16x16x128_f8f6f4 v[36:39], v[0:7], v[232:239], v[36:39]
	v_mfma_f32_16x16x128_f8f6f4 v[32:35], v[8:15], v[232:239], v[32:35]
	s_setprio 0
	s_barrier
	s_mov_b32 m0, s33
	s_nop 0
	global_load_lds_dwordx4 v160, s[42:43]
	s_mov_b32 m0, s48
	s_nop 0
	global_load_lds_dwordx4 v164, s[42:43]
	ds_read_b128 v[0:3], v197
	ds_read_b128 v[4:7], v198
	ds_read_b128 v[8:11], v199
	ds_read_b128 v[12:15], v200
	ds_read_b128 v[16:19], v201
	ds_read_b128 v[20:23], v202
	ds_read_b128 v[24:27], v203
	ds_read_b128 v[28:31], v204
	s_add_u32 s42, s42, 0x80000
	s_addc_u32 s43, s43, 0
	s_mov_b32 m0, s49
	ds_read_b128 v[208:211], v205 offset:32768
	ds_read_b128 v[212:215], v205 offset:33792
	ds_read_b128 v[216:219], v205 offset:34816
	ds_read_b128 v[220:223], v205 offset:35840
	ds_read_b128 v[224:227], v205 offset:36864
	ds_read_b128 v[228:231], v205 offset:37888
	ds_read_b128 v[232:235], v205 offset:38912
	ds_read_b128 v[236:239], v205 offset:39936
	global_load_lds_dwordx4 v160, s[42:43]
	s_mov_b32 m0, s50
	s_nop 0
	global_load_lds_dwordx4 v164, s[42:43]
	s_waitcnt vmcnt(8)
	s_waitcnt lgkmcnt(0)
	s_barrier
	s_setprio 1
	s_waitcnt lgkmcnt(0)
	v_mfma_f32_16x16x128_f8f6f4 v[156:159], v[0:7], v[208:215], v[156:159]
	v_mfma_f32_16x16x128_f8f6f4 v[152:155], v[8:15], v[208:215], v[152:155]
	v_mfma_f32_16x16x128_f8f6f4 v[140:143], v[0:7], v[216:223], v[140:143]
	v_mfma_f32_16x16x128_f8f6f4 v[136:139], v[8:15], v[216:223], v[136:139]
	v_mfma_f32_16x16x128_f8f6f4 v[124:127], v[0:7], v[224:231], v[124:127]
	v_mfma_f32_16x16x128_f8f6f4 v[120:123], v[8:15], v[224:231], v[120:123]
	v_mfma_f32_16x16x128_f8f6f4 v[108:111], v[0:7], v[232:239], v[108:111]
	v_mfma_f32_16x16x128_f8f6f4 v[104:107], v[8:15], v[232:239], v[104:107]
	s_setprio 0
	s_setprio 1
	v_mfma_f32_16x16x128_f8f6f4 v[148:151], v[16:23], v[208:215], v[148:151]
	v_mfma_f32_16x16x128_f8f6f4 v[144:147], v[24:31], v[208:215], v[144:147]
	v_mfma_f32_16x16x128_f8f6f4 v[132:135], v[16:23], v[216:223], v[132:135]
	v_mfma_f32_16x16x128_f8f6f4 v[128:131], v[24:31], v[216:223], v[128:131]
	v_mfma_f32_16x16x128_f8f6f4 v[116:119], v[16:23], v[224:231], v[116:119]
	v_mfma_f32_16x16x128_f8f6f4 v[112:115], v[24:31], v[224:231], v[112:115]
	v_mfma_f32_16x16x128_f8f6f4 v[100:103], v[16:23], v[232:239], v[100:103]
	v_mfma_f32_16x16x128_f8f6f4 v[96:99], v[24:31], v[232:239], v[96:99]
	s_setprio 0
	s_barrier
	s_mov_b32 m0, s51
	v_lshl_add_u64 v[180:181], v[180:181], 0, s[12:13]
	s_add_u32 s40, s40, 0x80080
	ds_read_b128 v[208:211], v205 offset:49152
	ds_read_b128 v[212:215], v205 offset:50176
	ds_read_b128 v[216:219], v205 offset:51200
	ds_read_b128 v[220:223], v205 offset:52224
	ds_read_b128 v[224:227], v205 offset:53248
	ds_read_b128 v[228:231], v205 offset:54272
	ds_read_b128 v[232:235], v205 offset:55296
	ds_read_b128 v[236:239], v205 offset:56320
	global_load_lds_dwordx4 v[180:181], off
	v_lshl_add_u64 v[180:181], v[182:183], 0, s[12:13]
	s_mov_b32 m0, s52
	s_addc_u32 s41, s41, 0
	global_load_lds_dwordx4 v[180:181], off
	s_mov_b32 m0, s55
	s_nop 0
	global_load_lds_dwordx4 v162, s[40:41]
	s_mov_b32 m0, s56
	s_nop 0
	global_load_lds_dwordx4 v166, s[40:41]
	s_waitcnt vmcnt(6)
	s_waitcnt lgkmcnt(0)
	s_barrier
	s_setprio 1
	s_waitcnt lgkmcnt(0)
	v_mfma_f32_16x16x128_f8f6f4 v[92:95], v[0:7], v[208:215], v[92:95]
	v_mfma_f32_16x16x128_f8f6f4 v[88:91], v[8:15], v[208:215], v[88:91]
	v_mfma_f32_16x16x128_f8f6f4 v[76:79], v[0:7], v[216:223], v[76:79]
	v_mfma_f32_16x16x128_f8f6f4 v[72:75], v[8:15], v[216:223], v[72:75]
	v_mfma_f32_16x16x128_f8f6f4 v[60:63], v[0:7], v[224:231], v[60:63]
	v_mfma_f32_16x16x128_f8f6f4 v[56:59], v[8:15], v[224:231], v[56:59]
	v_mfma_f32_16x16x128_f8f6f4 v[44:47], v[0:7], v[232:239], v[44:47]
	v_mfma_f32_16x16x128_f8f6f4 v[40:43], v[8:15], v[232:239], v[40:43]
	s_setprio 0
	s_setprio 1
	v_mfma_f32_16x16x128_f8f6f4 v[84:87], v[16:23], v[208:215], v[84:87]
	v_mfma_f32_16x16x128_f8f6f4 v[80:83], v[24:31], v[208:215], v[80:83]
	v_mfma_f32_16x16x128_f8f6f4 v[68:71], v[16:23], v[216:223], v[68:71]
	v_mfma_f32_16x16x128_f8f6f4 v[64:67], v[24:31], v[216:223], v[64:67]
	v_mfma_f32_16x16x128_f8f6f4 v[52:55], v[16:23], v[224:231], v[52:55]
	v_mfma_f32_16x16x128_f8f6f4 v[48:51], v[24:31], v[224:231], v[48:51]
	v_mfma_f32_16x16x128_f8f6f4 v[36:39], v[16:23], v[232:239], v[36:39]
	v_mfma_f32_16x16x128_f8f6f4 v[32:35], v[24:31], v[232:239], v[32:35]
	s_setprio 0
	s_barrier
	s_add_i32 s64, s64, 2
	s_add_u32 s38, s38, 0x100
	s_addc_u32 s39, s39, 0
	s_add_u32 s60, s60, 0x100
	s_addc_u32 s61, s61, 0
	s_cmp_gt_u32 s64, 29
	s_cbranch_scc0 .LBB0_940
	s_nop 15
	s_nop 15
	s_and_b64 vcc, exec, s[14:15]
	s_cbranch_vccz .LBB0_943
	s_barrier

.LBB0_1358:
	s_add_u32 s30, s26, 0x1000
	s_addc_u32 s31, s27, 0
	s_mov_b32 m0, s49
	s_nop 0
	global_load_lds_dwordx4 v160, s[30:31]
	s_mov_b32 m0, s50
	s_nop 0
	global_load_lds_dwordx4 v164, s[30:31]
	ds_read_b128 v[16:19], v207
	ds_read_b128 v[20:23], v208
	ds_read_b128 v[24:27], v209
	ds_read_b128 v[28:31], v210
	ds_read_b128 v[0:3], v211
	ds_read_b128 v[4:7], v212
	ds_read_b128 v[8:11], v213
	ds_read_b128 v[12:15], v214
	s_add_u32 s28, s26, 0x10000
	s_addc_u32 s29, s27, 0
	s_cmpk_eq_i32 s59, 0x7c
	s_cselect_b32 s36, s55, s28
	s_cselect_b32 s37, s19, s29
	s_cselect_b32 s34, s56, s57
	s_cselect_b32 s35, s17, s58
	s_add_i32 m0, s25, 0xc000
	ds_read_b128 v[176:179], v224
	ds_read_b128 v[180:183], v224 offset:1024
	ds_read_b128 v[184:187], v224 offset:2048
	ds_read_b128 v[188:191], v224 offset:3072
	ds_read_b128 v[192:195], v224 offset:4096
	ds_read_b128 v[196:199], v224 offset:5120
	ds_read_b128 v[226:229], v224 offset:6144
	ds_read_b128 v[230:233], v224 offset:7168
	global_load_lds_dwordx4 v168, s[26:27]
	s_add_i32 m0, s25, 0xe000
	s_nop 0
	global_load_lds_dwordx4 v170, s[26:27]
	s_waitcnt vmcnt(8)
	s_waitcnt lgkmcnt(0)
	s_barrier
	s_setprio 1
	s_waitcnt lgkmcnt(0)
	v_mfma_f32_16x16x128_f8f6f4 v[156:159], v[16:23], v[176:183], v[156:159]
	v_mfma_f32_16x16x128_f8f6f4 v[152:155], v[24:31], v[176:183], v[152:155]
	v_mfma_f32_16x16x128_f8f6f4 v[144:147], v[16:23], v[184:191], v[144:147]
	v_mfma_f32_16x16x128_f8f6f4 v[136:139], v[24:31], v[184:191], v[136:139]
	v_mfma_f32_16x16x128_f8f6f4 v[124:127], v[16:23], v[192:199], v[124:127]
	v_mfma_f32_16x16x128_f8f6f4 v[120:123], v[24:31], v[192:199], v[120:123]
	v_mfma_f32_16x16x128_f8f6f4 v[112:115], v[16:23], v[226:233], v[112:115]
	v_mfma_f32_16x16x128_f8f6f4 v[104:107], v[24:31], v[226:233], v[104:107]
	s_setprio 0
	s_setprio 1
	v_mfma_f32_16x16x128_f8f6f4 v[148:151], v[0:7], v[176:183], v[148:151]
	v_mfma_f32_16x16x128_f8f6f4 v[140:143], v[8:15], v[176:183], v[140:143]
	v_mfma_f32_16x16x128_f8f6f4 v[132:135], v[0:7], v[184:191], v[132:135]
	v_mfma_f32_16x16x128_f8f6f4 v[128:131], v[8:15], v[184:191], v[128:131]
	v_mfma_f32_16x16x128_f8f6f4 v[116:119], v[0:7], v[192:199], v[116:119]
	v_mfma_f32_16x16x128_f8f6f4 v[108:111], v[8:15], v[192:199], v[108:111]
	v_mfma_f32_16x16x128_f8f6f4 v[100:103], v[0:7], v[226:233], v[100:103]
	v_mfma_f32_16x16x128_f8f6f4 v[96:99], v[8:15], v[226:233], v[96:99]
	s_setprio 0
	s_barrier
	s_mov_b32 m0, s33
	v_lshl_add_u64 v[176:177], s[34:35], 0, v[162:163]
	s_add_u32 s26, s34, 0x200000
	ds_read_b128 v[180:183], v224 offset:16384
	ds_read_b128 v[184:187], v224 offset:17408
	ds_read_b128 v[188:191], v224 offset:18432
	ds_read_b128 v[192:195], v224 offset:19456
	ds_read_b128 v[196:199], v224 offset:20480
	ds_read_b128 v[200:203], v224 offset:21504
	ds_read_b128 v[226:229], v224 offset:22528
	ds_read_b128 v[230:233], v224 offset:23552
	global_load_lds_dwordx4 v[176:177], off
	v_lshl_add_u64 v[178:179], s[34:35], 0, v[166:167]
	s_mov_b32 m0, s38
	s_addc_u32 s27, s35, 0
	global_load_lds_dwordx4 v[178:179], off
	s_mov_b32 m0, s39
	s_nop 0
	global_load_lds_dwordx4 v162, s[26:27]
	s_mov_b32 m0, s40
	s_nop 0
	global_load_lds_dwordx4 v166, s[26:27]
	s_waitcnt vmcnt(6)
	s_waitcnt lgkmcnt(0)
	s_barrier
	s_setprio 1
	s_waitcnt lgkmcnt(0)
	v_mfma_f32_16x16x128_f8f6f4 v[92:95], v[16:23], v[180:187], v[92:95]
	v_mfma_f32_16x16x128_f8f6f4 v[88:91], v[24:31], v[180:187], v[88:91]
	v_mfma_f32_16x16x128_f8f6f4 v[80:83], v[16:23], v[188:195], v[80:83]
	v_mfma_f32_16x16x128_f8f6f4 v[72:75], v[24:31], v[188:195], v[72:75]
	v_mfma_f32_16x16x128_f8f6f4 v[64:67], v[16:23], v[196:203], v[64:67]
	v_mfma_f32_16x16x128_f8f6f4 v[56:59], v[24:31], v[196:203], v[56:59]
	v_mfma_f32_16x16x128_f8f6f4 v[48:51], v[16:23], v[226:233], v[48:51]
	v_mfma_f32_16x16x128_f8f6f4 v[40:43], v[24:31], v[226:233], v[40:43]
	s_setprio 0
	s_setprio 1
	v_mfma_f32_16x16x128_f8f6f4 v[84:87], v[0:7], v[180:187], v[84:87]
	v_mfma_f32_16x16x128_f8f6f4 v[76:79], v[8:15], v[180:187], v[76:79]
	v_mfma_f32_16x16x128_f8f6f4 v[68:71], v[0:7], v[188:195], v[68:71]
	v_mfma_f32_16x16x128_f8f6f4 v[60:63], v[8:15], v[188:195], v[60:63]
	v_mfma_f32_16x16x128_f8f6f4 v[52:55], v[0:7], v[196:203], v[52:55]
	v_mfma_f32_16x16x128_f8f6f4 v[44:47], v[8:15], v[196:203], v[44:47]
	v_mfma_f32_16x16x128_f8f6f4 v[36:39], v[0:7], v[226:233], v[36:39]
	v_mfma_f32_16x16x128_f8f6f4 v[32:35], v[8:15], v[226:233], v[32:35]
	s_setprio 0
	s_barrier
	s_mov_b32 m0, s25
	s_nop 0
	global_load_lds_dwordx4 v160, s[36:37]
	s_mov_b32 m0, s41
	s_nop 0
	global_load_lds_dwordx4 v164, s[36:37]
	ds_read_b128 v[0:3], v215
	ds_read_b128 v[4:7], v216
	ds_read_b128 v[8:11], v217
	ds_read_b128 v[12:15], v218
	ds_read_b128 v[16:19], v219
	ds_read_b128 v[20:23], v220
	ds_read_b128 v[24:27], v221
	ds_read_b128 v[28:31], v222
	s_add_u32 s26, s36, 0x8000
	s_addc_u32 s27, s37, 0
	s_mov_b32 m0, s42
	ds_read_b128 v[180:183], v224 offset:32768
	ds_read_b128 v[184:187], v224 offset:33792
	ds_read_b128 v[188:191], v224 offset:34816
	ds_read_b128 v[192:195], v224 offset:35840
	ds_read_b128 v[196:199], v224 offset:36864
	ds_read_b128 v[200:203], v224 offset:37888
	ds_read_b128 v[226:229], v224 offset:38912
	ds_read_b128 v[230:233], v224 offset:39936
	global_load_lds_dwordx4 v160, s[26:27]
	s_mov_b32 m0, s43
	s_nop 0
	global_load_lds_dwordx4 v164, s[26:27]
	s_waitcnt vmcnt(8)
	s_waitcnt lgkmcnt(0)
	s_barrier
	s_setprio 1
	s_waitcnt lgkmcnt(0)
	v_mfma_f32_16x16x128_f8f6f4 v[156:159], v[0:7], v[180:187], v[156:159]
	v_mfma_f32_16x16x128_f8f6f4 v[152:155], v[8:15], v[180:187], v[152:155]
	v_mfma_f32_16x16x128_f8f6f4 v[144:147], v[0:7], v[188:195], v[144:147]
	v_mfma_f32_16x16x128_f8f6f4 v[136:139], v[8:15], v[188:195], v[136:139]
	v_mfma_f32_16x16x128_f8f6f4 v[124:127], v[0:7], v[196:203], v[124:127]
	v_mfma_f32_16x16x128_f8f6f4 v[120:123], v[8:15], v[196:203], v[120:123]
	v_mfma_f32_16x16x128_f8f6f4 v[112:115], v[0:7], v[226:233], v[112:115]
	v_mfma_f32_16x16x128_f8f6f4 v[104:107], v[8:15], v[226:233], v[104:107]
	s_setprio 0
	s_setprio 1
	v_mfma_f32_16x16x128_f8f6f4 v[148:151], v[16:23], v[180:187], v[148:151]
	v_mfma_f32_16x16x128_f8f6f4 v[140:143], v[24:31], v[180:187], v[140:143]
	v_mfma_f32_16x16x128_f8f6f4 v[132:135], v[16:23], v[188:195], v[132:135]
	v_mfma_f32_16x16x128_f8f6f4 v[128:131], v[24:31], v[188:195], v[128:131]
	v_mfma_f32_16x16x128_f8f6f4 v[116:119], v[16:23], v[196:203], v[116:119]
	v_mfma_f32_16x16x128_f8f6f4 v[108:111], v[24:31], v[196:203], v[108:111]
	v_mfma_f32_16x16x128_f8f6f4 v[100:103], v[16:23], v[226:233], v[100:103]
	v_mfma_f32_16x16x128_f8f6f4 v[96:99], v[24:31], v[226:233], v[96:99]
	s_setprio 0
	s_barrier
	s_mov_b32 m0, s47
	v_lshl_add_u64 v[176:177], v[176:177], 0, s[10:11]
	s_add_u32 s26, s34, 0x200080
	ds_read_b128 v[180:183], v224 offset:49152
	ds_read_b128 v[184:187], v224 offset:50176
	ds_read_b128 v[188:191], v224 offset:51200
	ds_read_b128 v[192:195], v224 offset:52224
	ds_read_b128 v[196:199], v224 offset:53248
	ds_read_b128 v[200:203], v224 offset:54272
	ds_read_b128 v[226:229], v224 offset:55296
	ds_read_b128 v[230:233], v224 offset:56320
	global_load_lds_dwordx4 v[176:177], off
	v_lshl_add_u64 v[176:177], v[178:179], 0, s[10:11]
	s_mov_b32 m0, s48
	s_addc_u32 s27, s35, 0
	global_load_lds_dwordx4 v[176:177], off
	s_mov_b32 m0, s51
	s_nop 0
	global_load_lds_dwordx4 v162, s[26:27]
	s_mov_b32 m0, s52
	s_nop 0
	global_load_lds_dwordx4 v166, s[26:27]
	s_waitcnt vmcnt(6)
	s_waitcnt lgkmcnt(0)
	s_barrier
	s_setprio 1
	s_waitcnt lgkmcnt(0)
	v_mfma_f32_16x16x128_f8f6f4 v[92:95], v[0:7], v[180:187], v[92:95]
	v_mfma_f32_16x16x128_f8f6f4 v[88:91], v[8:15], v[180:187], v[88:91]
	v_mfma_f32_16x16x128_f8f6f4 v[80:83], v[0:7], v[188:195], v[80:83]
	v_mfma_f32_16x16x128_f8f6f4 v[72:75], v[8:15], v[188:195], v[72:75]
	v_mfma_f32_16x16x128_f8f6f4 v[64:67], v[0:7], v[196:203], v[64:67]
	v_mfma_f32_16x16x128_f8f6f4 v[56:59], v[8:15], v[196:203], v[56:59]
	v_mfma_f32_16x16x128_f8f6f4 v[48:51], v[0:7], v[226:233], v[48:51]
	v_mfma_f32_16x16x128_f8f6f4 v[40:43], v[8:15], v[226:233], v[40:43]
	s_setprio 0
	s_setprio 1
	v_mfma_f32_16x16x128_f8f6f4 v[84:87], v[16:23], v[180:187], v[84:87]
	v_mfma_f32_16x16x128_f8f6f4 v[76:79], v[24:31], v[180:187], v[76:79]
	v_mfma_f32_16x16x128_f8f6f4 v[68:71], v[16:23], v[188:195], v[68:71]
	v_mfma_f32_16x16x128_f8f6f4 v[60:63], v[24:31], v[188:195], v[60:63]
	v_mfma_f32_16x16x128_f8f6f4 v[52:55], v[16:23], v[196:203], v[52:55]
	v_mfma_f32_16x16x128_f8f6f4 v[44:47], v[24:31], v[196:203], v[44:47]
	v_mfma_f32_16x16x128_f8f6f4 v[36:39], v[16:23], v[226:233], v[36:39]
	v_mfma_f32_16x16x128_f8f6f4 v[32:35], v[24:31], v[226:233], v[32:35]
	s_setprio 0
	s_barrier
	s_add_i32 s59, s59, 2
	s_add_u32 s57, s57, 0x100
	s_addc_u32 s58, s58, 0
	s_cmpk_gt_u32 s59, 0x7d
	s_mov_b64 s[26:27], s[28:29]
	s_cbranch_scc0 .LBB0_1358
	s_nop 15
	s_nop 15
	s_and_b64 vcc, exec, s[12:13]
	s_cbranch_vccz .LBB0_1361
	s_barrier
